# lever 7 (instruction selection): moe-up SwiGLU epilogue re-emitted with packed f32 mul/add for the scale and +1 steps (36 VALU per 8 outputs instead of 44), one address base
# baseline (speedup 1.0000x reference)
.LBB0_1428:
	s_lshl_b32 s2, s61, 8
	v_mbcnt_lo_u32_b32 v133, -1, 0
	v_mbcnt_hi_u32_b32 v133, -1, v133
	s_add_i32 s2, s2, s49
	v_and_or_b32 v132, v133, 15, s2
	s_lshl_b32 s2, s62, 7
	v_ashrrev_i32_e32 v133, 1, v133
	s_or_b32 s2, s2, s50
	v_and_b32_e32 v133, -8, v133
	v_add_u32_e32 v142, s2, v133
	v_ashrrev_i32_e32 v143, 31, v142
	v_ashrrev_i32_e32 v133, 31, v132
	v_lshlrev_b64 v[146:147], 11, v[132:133]
	v_lshl_add_u64 v[146:147], s[12:13], 0, v[146:147]
	v_lshlrev_b64 v[148:149], 1, v[142:143]
	v_lshl_add_u64 v[178:179], v[146:147], 0, v[148:149]
	s_mov_b32 s100, 0xbfb8aa3b
	v_pk_mul_f32 v[150:151], v[128:129], s[100:101] op_sel_hi:[1,0]
	v_pk_mul_f32 v[152:153], v[130:131], s[100:101] op_sel_hi:[1,0]
	v_pk_mul_f32 v[154:155], v[116:117], s[100:101] op_sel_hi:[1,0]
	v_pk_mul_f32 v[156:157], v[118:119], s[100:101] op_sel_hi:[1,0]
	v_exp_f32_e32 v150, v150
	v_exp_f32_e32 v151, v151
	v_exp_f32_e32 v152, v152
	v_exp_f32_e32 v153, v153
	v_exp_f32_e32 v154, v154
	v_exp_f32_e32 v155, v155
	v_exp_f32_e32 v156, v156
	v_exp_f32_e32 v157, v157
	v_pk_add_f32 v[150:151], v[150:151], 1.0 op_sel_hi:[1,0]
	v_pk_add_f32 v[152:153], v[152:153], 1.0 op_sel_hi:[1,0]
	v_pk_add_f32 v[154:155], v[154:155], 1.0 op_sel_hi:[1,0]
	v_pk_add_f32 v[156:157], v[156:157], 1.0 op_sel_hi:[1,0]
	v_rcp_f32_e32 v150, v150
	v_rcp_f32_e32 v151, v151
	v_rcp_f32_e32 v152, v152
	v_rcp_f32_e32 v153, v153
	v_rcp_f32_e32 v154, v154
	v_rcp_f32_e32 v155, v155
	v_rcp_f32_e32 v156, v156
	v_rcp_f32_e32 v157, v157
	v_pk_mul_f32 v[150:151], v[128:129], v[150:151]
	v_pk_mul_f32 v[152:153], v[130:131], v[152:153]
	v_pk_mul_f32 v[154:155], v[116:117], v[154:155]
	v_pk_mul_f32 v[156:157], v[118:119], v[156:157]
	v_pk_mul_f32 v[150:151], v[150:151], v[124:125]
	v_pk_mul_f32 v[152:153], v[152:153], v[126:127]
	v_pk_mul_f32 v[154:155], v[154:155], v[120:121]
	v_pk_mul_f32 v[156:157], v[156:157], v[122:123]
	v_cvt_pk_bf16_f32 v158, v150, v151
	v_cvt_pk_bf16_f32 v159, v152, v153
	v_cvt_pk_bf16_f32 v160, v154, v155
	v_cvt_pk_bf16_f32 v161, v156, v157
	global_store_dwordx4 v[178:179], v[158:161], off
	v_pk_mul_f32 v[164:165], v[110:111], s[100:101] op_sel_hi:[1,0]
	v_pk_mul_f32 v[166:167], v[112:113], s[100:101] op_sel_hi:[1,0]
	v_pk_mul_f32 v[168:169], v[98:99], s[100:101] op_sel_hi:[1,0]
	v_pk_mul_f32 v[170:171], v[100:101], s[100:101] op_sel_hi:[1,0]
	v_exp_f32_e32 v164, v164
	v_exp_f32_e32 v165, v165
	v_exp_f32_e32 v166, v166
	v_exp_f32_e32 v167, v167
	v_exp_f32_e32 v168, v168
	v_exp_f32_e32 v169, v169
	v_exp_f32_e32 v170, v170
	v_exp_f32_e32 v171, v171
	v_pk_add_f32 v[164:165], v[164:165], 1.0 op_sel_hi:[1,0]
	v_pk_add_f32 v[166:167], v[166:167], 1.0 op_sel_hi:[1,0]
	v_pk_add_f32 v[168:169], v[168:169], 1.0 op_sel_hi:[1,0]
	v_pk_add_f32 v[170:171], v[170:171], 1.0 op_sel_hi:[1,0]
	v_rcp_f32_e32 v164, v164
	v_rcp_f32_e32 v165, v165
	v_rcp_f32_e32 v166, v166
	v_rcp_f32_e32 v167, v167
	v_rcp_f32_e32 v168, v168
	v_rcp_f32_e32 v169, v169
	v_rcp_f32_e32 v170, v170
	v_rcp_f32_e32 v171, v171
	v_pk_mul_f32 v[164:165], v[110:111], v[164:165]
	v_pk_mul_f32 v[166:167], v[112:113], v[166:167]
	v_pk_mul_f32 v[168:169], v[98:99], v[168:169]
	v_pk_mul_f32 v[170:171], v[100:101], v[170:171]
	v_pk_mul_f32 v[164:165], v[164:165], v[106:107]
	v_pk_mul_f32 v[166:167], v[166:167], v[108:109]
	v_pk_mul_f32 v[168:169], v[168:169], v[102:103]
	v_pk_mul_f32 v[170:171], v[170:171], v[104:105]
	v_cvt_pk_bf16_f32 v172, v164, v165
	v_cvt_pk_bf16_f32 v173, v166, v167
	v_cvt_pk_bf16_f32 v174, v168, v169
	v_cvt_pk_bf16_f32 v175, v170, v171
	v_add_co_u32_e32 v176, vcc, 0x8000, v178
	s_nop 0
	v_addc_co_u32_e32 v177, vcc, 0, v179, vcc
	global_store_dwordx4 v[176:177], v[172:175], off
	v_pk_mul_f32 v[150:151], v[94:95], s[100:101] op_sel_hi:[1,0]
	v_pk_mul_f32 v[152:153], v[96:97], s[100:101] op_sel_hi:[1,0]
	v_pk_mul_f32 v[154:155], v[82:83], s[100:101] op_sel_hi:[1,0]
	v_pk_mul_f32 v[156:157], v[84:85], s[100:101] op_sel_hi:[1,0]
	v_exp_f32_e32 v150, v150
	v_exp_f32_e32 v151, v151
	v_exp_f32_e32 v152, v152
	v_exp_f32_e32 v153, v153
	v_exp_f32_e32 v154, v154
	v_exp_f32_e32 v155, v155
	v_exp_f32_e32 v156, v156
	v_exp_f32_e32 v157, v157
	v_pk_add_f32 v[150:151], v[150:151], 1.0 op_sel_hi:[1,0]
	v_pk_add_f32 v[152:153], v[152:153], 1.0 op_sel_hi:[1,0]
	v_pk_add_f32 v[154:155], v[154:155], 1.0 op_sel_hi:[1,0]
	v_pk_add_f32 v[156:157], v[156:157], 1.0 op_sel_hi:[1,0]
	v_rcp_f32_e32 v150, v150
	v_rcp_f32_e32 v151, v151
	v_rcp_f32_e32 v152, v152
	v_rcp_f32_e32 v153, v153
	v_rcp_f32_e32 v154, v154
	v_rcp_f32_e32 v155, v155
	v_rcp_f32_e32 v156, v156
	v_rcp_f32_e32 v157, v157
	v_pk_mul_f32 v[150:151], v[94:95], v[150:151]
	v_pk_mul_f32 v[152:153], v[96:97], v[152:153]
	v_pk_mul_f32 v[154:155], v[82:83], v[154:155]
	v_pk_mul_f32 v[156:157], v[84:85], v[156:157]
	v_pk_mul_f32 v[150:151], v[150:151], v[90:91]
	v_pk_mul_f32 v[152:153], v[152:153], v[92:93]
	v_pk_mul_f32 v[154:155], v[154:155], v[86:87]
	v_pk_mul_f32 v[156:157], v[156:157], v[88:89]
	v_cvt_pk_bf16_f32 v158, v150, v151
	v_cvt_pk_bf16_f32 v159, v152, v153
	v_cvt_pk_bf16_f32 v160, v154, v155
	v_cvt_pk_bf16_f32 v161, v156, v157
	v_add_co_u32_e32 v162, vcc, 0x10000, v178
	s_nop 0
	v_addc_co_u32_e32 v163, vcc, 0, v179, vcc
	global_store_dwordx4 v[162:163], v[158:161], off
	v_pk_mul_f32 v[164:165], v[78:79], s[100:101] op_sel_hi:[1,0]
	v_pk_mul_f32 v[166:167], v[80:81], s[100:101] op_sel_hi:[1,0]
	v_pk_mul_f32 v[168:169], v[56:57], s[100:101] op_sel_hi:[1,0]
	v_pk_mul_f32 v[170:171], v[58:59], s[100:101] op_sel_hi:[1,0]
	v_exp_f32_e32 v164, v164
	v_exp_f32_e32 v165, v165
	v_exp_f32_e32 v166, v166
	v_exp_f32_e32 v167, v167
	v_exp_f32_e32 v168, v168
	v_exp_f32_e32 v169, v169
	v_exp_f32_e32 v170, v170
	v_exp_f32_e32 v171, v171
	v_pk_add_f32 v[164:165], v[164:165], 1.0 op_sel_hi:[1,0]
	v_pk_add_f32 v[166:167], v[166:167], 1.0 op_sel_hi:[1,0]
	v_pk_add_f32 v[168:169], v[168:169], 1.0 op_sel_hi:[1,0]
	v_pk_add_f32 v[170:171], v[170:171], 1.0 op_sel_hi:[1,0]
	v_rcp_f32_e32 v164, v164
	v_rcp_f32_e32 v165, v165
	v_rcp_f32_e32 v166, v166
	v_rcp_f32_e32 v167, v167
	v_rcp_f32_e32 v168, v168
	v_rcp_f32_e32 v169, v169
	v_rcp_f32_e32 v170, v170
	v_rcp_f32_e32 v171, v171
	v_pk_mul_f32 v[164:165], v[78:79], v[164:165]
	v_pk_mul_f32 v[166:167], v[80:81], v[166:167]
	v_pk_mul_f32 v[168:169], v[56:57], v[168:169]
	v_pk_mul_f32 v[170:171], v[58:59], v[170:171]
	v_pk_mul_f32 v[164:165], v[164:165], v[74:75]
	v_pk_mul_f32 v[166:167], v[166:167], v[76:77]
	v_pk_mul_f32 v[168:169], v[168:169], v[70:71]
	v_pk_mul_f32 v[170:171], v[170:171], v[72:73]
	v_cvt_pk_bf16_f32 v172, v164, v165
	v_cvt_pk_bf16_f32 v173, v166, v167
	v_cvt_pk_bf16_f32 v174, v168, v169
	v_cvt_pk_bf16_f32 v175, v170, v171
	v_add_co_u32_e32 v176, vcc, 0x18000, v178
	s_nop 0
	v_addc_co_u32_e32 v177, vcc, 0, v179, vcc
	global_store_dwordx4 v[176:177], v[172:175], off
	v_pk_mul_f32 v[150:151], v[66:67], s[100:101] op_sel_hi:[1,0]
	v_pk_mul_f32 v[152:153], v[68:69], s[100:101] op_sel_hi:[1,0]
	v_pk_mul_f32 v[154:155], v[48:49], s[100:101] op_sel_hi:[1,0]
	v_pk_mul_f32 v[156:157], v[50:51], s[100:101] op_sel_hi:[1,0]
	v_exp_f32_e32 v150, v150
	v_exp_f32_e32 v151, v151
	v_exp_f32_e32 v152, v152
	v_exp_f32_e32 v153, v153
	v_exp_f32_e32 v154, v154
	v_exp_f32_e32 v155, v155
	v_exp_f32_e32 v156, v156
	v_exp_f32_e32 v157, v157
	v_pk_add_f32 v[150:151], v[150:151], 1.0 op_sel_hi:[1,0]
	v_pk_add_f32 v[152:153], v[152:153], 1.0 op_sel_hi:[1,0]
	v_pk_add_f32 v[154:155], v[154:155], 1.0 op_sel_hi:[1,0]
	v_pk_add_f32 v[156:157], v[156:157], 1.0 op_sel_hi:[1,0]
	v_rcp_f32_e32 v150, v150
	v_rcp_f32_e32 v151, v151
	v_rcp_f32_e32 v152, v152
	v_rcp_f32_e32 v153, v153
	v_rcp_f32_e32 v154, v154
	v_rcp_f32_e32 v155, v155
	v_rcp_f32_e32 v156, v156
	v_rcp_f32_e32 v157, v157
	v_pk_mul_f32 v[150:151], v[66:67], v[150:151]
	v_pk_mul_f32 v[152:153], v[68:69], v[152:153]
	v_pk_mul_f32 v[154:155], v[48:49], v[154:155]
	v_pk_mul_f32 v[156:157], v[50:51], v[156:157]
	v_pk_mul_f32 v[150:151], v[150:151], v[60:61]
	v_pk_mul_f32 v[152:153], v[152:153], v[62:63]
	v_pk_mul_f32 v[154:155], v[154:155], v[52:53]
	v_pk_mul_f32 v[156:157], v[156:157], v[54:55]
	v_cvt_pk_bf16_f32 v158, v150, v151
	v_cvt_pk_bf16_f32 v159, v152, v153
	v_cvt_pk_bf16_f32 v160, v154, v155
	v_cvt_pk_bf16_f32 v161, v156, v157
	v_add_co_u32_e32 v162, vcc, 0x40000, v178
	s_nop 0
	v_addc_co_u32_e32 v163, vcc, 0, v179, vcc
	global_store_dwordx4 v[162:163], v[158:161], off
	v_pk_mul_f32 v[164:165], v[44:45], s[100:101] op_sel_hi:[1,0]
	v_pk_mul_f32 v[166:167], v[46:47], s[100:101] op_sel_hi:[1,0]
	v_pk_mul_f32 v[168:169], v[32:33], s[100:101] op_sel_hi:[1,0]
	v_pk_mul_f32 v[170:171], v[34:35], s[100:101] op_sel_hi:[1,0]
	v_exp_f32_e32 v164, v164
	v_exp_f32_e32 v165, v165
	v_exp_f32_e32 v166, v166
	v_exp_f32_e32 v167, v167
	v_exp_f32_e32 v168, v168
	v_exp_f32_e32 v169, v169
	v_exp_f32_e32 v170, v170
	v_exp_f32_e32 v171, v171
	v_pk_add_f32 v[164:165], v[164:165], 1.0 op_sel_hi:[1,0]
	v_pk_add_f32 v[166:167], v[166:167], 1.0 op_sel_hi:[1,0]
	v_pk_add_f32 v[168:169], v[168:169], 1.0 op_sel_hi:[1,0]
	v_pk_add_f32 v[170:171], v[170:171], 1.0 op_sel_hi:[1,0]
	v_rcp_f32_e32 v164, v164
	v_rcp_f32_e32 v165, v165
	v_rcp_f32_e32 v166, v166
	v_rcp_f32_e32 v167, v167
	v_rcp_f32_e32 v168, v168
	v_rcp_f32_e32 v169, v169
	v_rcp_f32_e32 v170, v170
	v_rcp_f32_e32 v171, v171
	v_pk_mul_f32 v[164:165], v[44:45], v[164:165]
	v_pk_mul_f32 v[166:167], v[46:47], v[166:167]
	v_pk_mul_f32 v[168:169], v[32:33], v[168:169]
	v_pk_mul_f32 v[170:171], v[34:35], v[170:171]
	v_pk_mul_f32 v[164:165], v[164:165], v[40:41]
	v_pk_mul_f32 v[166:167], v[166:167], v[42:43]
	v_pk_mul_f32 v[168:169], v[168:169], v[36:37]
	v_pk_mul_f32 v[170:171], v[170:171], v[38:39]
	v_cvt_pk_bf16_f32 v172, v164, v165
	v_cvt_pk_bf16_f32 v173, v166, v167
	v_cvt_pk_bf16_f32 v174, v168, v169
	v_cvt_pk_bf16_f32 v175, v170, v171
	v_add_co_u32_e32 v176, vcc, 0x48000, v178
	s_nop 0
	v_addc_co_u32_e32 v177, vcc, 0, v179, vcc
	global_store_dwordx4 v[176:177], v[172:175], off
	v_pk_mul_f32 v[150:151], v[28:29], s[100:101] op_sel_hi:[1,0]
	v_pk_mul_f32 v[152:153], v[30:31], s[100:101] op_sel_hi:[1,0]
	v_pk_mul_f32 v[154:155], v[16:17], s[100:101] op_sel_hi:[1,0]
	v_pk_mul_f32 v[156:157], v[18:19], s[100:101] op_sel_hi:[1,0]
	v_exp_f32_e32 v150, v150
	v_exp_f32_e32 v151, v151
	v_exp_f32_e32 v152, v152
	v_exp_f32_e32 v153, v153
	v_exp_f32_e32 v154, v154
	v_exp_f32_e32 v155, v155
	v_exp_f32_e32 v156, v156
	v_exp_f32_e32 v157, v157
	v_pk_add_f32 v[150:151], v[150:151], 1.0 op_sel_hi:[1,0]
	v_pk_add_f32 v[152:153], v[152:153], 1.0 op_sel_hi:[1,0]
	v_pk_add_f32 v[154:155], v[154:155], 1.0 op_sel_hi:[1,0]
	v_pk_add_f32 v[156:157], v[156:157], 1.0 op_sel_hi:[1,0]
	v_rcp_f32_e32 v150, v150
	v_rcp_f32_e32 v151, v151
	v_rcp_f32_e32 v152, v152
	v_rcp_f32_e32 v153, v153
	v_rcp_f32_e32 v154, v154
	v_rcp_f32_e32 v155, v155
	v_rcp_f32_e32 v156, v156
	v_rcp_f32_e32 v157, v157
	v_pk_mul_f32 v[150:151], v[28:29], v[150:151]
	v_pk_mul_f32 v[152:153], v[30:31], v[152:153]
	v_pk_mul_f32 v[154:155], v[16:17], v[154:155]
	v_pk_mul_f32 v[156:157], v[18:19], v[156:157]
	v_pk_mul_f32 v[150:151], v[150:151], v[24:25]
	v_pk_mul_f32 v[152:153], v[152:153], v[26:27]
	v_pk_mul_f32 v[154:155], v[154:155], v[20:21]
	v_pk_mul_f32 v[156:157], v[156:157], v[22:23]
	v_cvt_pk_bf16_f32 v158, v150, v151
	v_cvt_pk_bf16_f32 v159, v152, v153
	v_cvt_pk_bf16_f32 v160, v154, v155
	v_cvt_pk_bf16_f32 v161, v156, v157
	v_add_co_u32_e32 v162, vcc, 0x50000, v178
	s_nop 0
	v_addc_co_u32_e32 v163, vcc, 0, v179, vcc
	global_store_dwordx4 v[162:163], v[158:161], off
	v_pk_mul_f32 v[164:165], v[12:13], s[100:101] op_sel_hi:[1,0]
	v_pk_mul_f32 v[166:167], v[14:15], s[100:101] op_sel_hi:[1,0]
	v_pk_mul_f32 v[168:169], v[0:1], s[100:101] op_sel_hi:[1,0]
	v_pk_mul_f32 v[170:171], v[2:3], s[100:101] op_sel_hi:[1,0]
	v_exp_f32_e32 v164, v164
	v_exp_f32_e32 v165, v165
	v_exp_f32_e32 v166, v166
	v_exp_f32_e32 v167, v167
	v_exp_f32_e32 v168, v168
	v_exp_f32_e32 v169, v169
	v_exp_f32_e32 v170, v170
	v_exp_f32_e32 v171, v171
	v_pk_add_f32 v[164:165], v[164:165], 1.0 op_sel_hi:[1,0]
	v_pk_add_f32 v[166:167], v[166:167], 1.0 op_sel_hi:[1,0]
	v_pk_add_f32 v[168:169], v[168:169], 1.0 op_sel_hi:[1,0]
	v_pk_add_f32 v[170:171], v[170:171], 1.0 op_sel_hi:[1,0]
	v_rcp_f32_e32 v164, v164
	v_rcp_f32_e32 v165, v165
	v_rcp_f32_e32 v166, v166
	v_rcp_f32_e32 v167, v167
	v_rcp_f32_e32 v168, v168
	v_rcp_f32_e32 v169, v169
	v_rcp_f32_e32 v170, v170
	v_rcp_f32_e32 v171, v171
	v_pk_mul_f32 v[164:165], v[12:13], v[164:165]
	v_pk_mul_f32 v[166:167], v[14:15], v[166:167]
	v_pk_mul_f32 v[168:169], v[0:1], v[168:169]
	v_pk_mul_f32 v[170:171], v[2:3], v[170:171]
	v_pk_mul_f32 v[164:165], v[164:165], v[8:9]
	v_pk_mul_f32 v[166:167], v[166:167], v[10:11]
	v_pk_mul_f32 v[168:169], v[168:169], v[4:5]
	v_pk_mul_f32 v[170:171], v[170:171], v[6:7]
	v_cvt_pk_bf16_f32 v172, v164, v165
	v_cvt_pk_bf16_f32 v173, v166, v167
	v_cvt_pk_bf16_f32 v174, v168, v169
	v_cvt_pk_bf16_f32 v175, v170, v171
	v_add_co_u32_e32 v176, vcc, 0x58000, v178
	s_nop 0
	v_addc_co_u32_e32 v177, vcc, 0, v179, vcc
	s_and_b64 vcc, exec, s[0:1]
	s_mov_b64 s[0:1], -1
	global_store_dwordx4 v[176:177], v[172:175], off
	s_cbranch_vccnz .LBB0_1417
	s_andn2_b64 vcc, exec, s[10:11]
	s_cbranch_vccnz .LBB0_1416
	s_barrier
	s_branch .LBB0_1416
